# mixer C unit header: Q loads no longer waited for before the workgroup barrier (vmcnt(16) before their first use instead)
# baseline (speedup 1.0000x reference)
; __device__ __forceinline__ void mixer_c_shared(const bf16* CQ, const bf16* CK, const bf16* CV  , bf16* O, const float* rel_bias, const float* sink, LAS unsigned char* lds, int G, int blk, int tid, int lane, int wave) {
;     ...
;         const int kvh = su & 3, v = su >> 2, b = v >> 5, q0 = 256 * (v & 31), w0 = q0 - 128;
;         const size_t tb0 = (size_t)b * SEQ;
;         const int i5 = lane & 31, hh = lane >> 5, q0w = q0 + 32 * wave, tq = q0w + i5;
;         const bf16* qp = CQ + (tb0 + tq) * 1024 + (4 * kvh) * 64 + 8 * hh;
;         bf16x8 qn[4];
; #pragma unroll
;         for (int d0 = 0; d0 < 4; ++d0) qn[d0] = *(const bf16x8*)(qp + 16 * d0);
;         __syncthreads();
.LBB0_1118:
	s_lshl_b32 s9, s39, 6
	s_ashr_i32 s8, s39, 7
	s_and_b32 s41, s9, 0x1f00
	s_ashr_i32 s9, s8, 31
	s_add_i32 s33, s41, s19
	s_lshl_b64 s[10:11], s[8:9], 13
	v_or_b32_e32 v4, s33, v139
	v_mov_b32_e32 v5, v3
	v_lshl_add_u64 v[6:7], s[10:11], 0, v[4:5]
	v_readlane_b32 s8, v255, 7
	s_and_b32 s40, s39, 3
	v_lshlrev_b64 v[8:9], 11, v[6:7]
	v_readlane_b32 s9, v255, 8
	s_lshl_b32 s16, s40, 9
	v_lshlrev_b32_e32 v2, 1, v138
	v_lshl_add_u64 v[8:9], s[8:9], 0, v[8:9]
	v_lshl_add_u64 v[8:9], v[8:9], 0, s[16:17]
	v_lshl_add_u64 v[144:145], v[8:9], 0, v[2:3]
	global_load_dwordx4 v[102:105], v[144:145], off
	global_load_dwordx4 v[106:109], v[144:145], off offset:32
	global_load_dwordx4 v[110:113], v[144:145], off offset:64
	global_load_dwordx4 v[114:117], v[144:145], off offset:96
	s_waitcnt lgkmcnt(0)
	s_barrier
	s_and_saveexec_b64 s[22:23], s[2:3]
	s_cbranch_execz .LBB0_1131
	s_lshl_b32 s16, s40, 7
	s_mov_b64 s[24:25], 0
	v_mov_b32_e32 v5, v173
	v_mov_b32_e32 v10, v1
	s_branch .LBB0_1121

; #define LAS __attribute__((address_space(3)))
; __device__ __forceinline__ void mixer_c_shared(const bf16* CQ, const bf16* CK, const bf16* CV  , bf16* O, const float* rel_bias, const float* sink, LAS unsigned char* lds, int G, int blk, int tid, int lane, int wave) {
;     ...
;         for (int idx = tid; idx < TC_LEN; idx += NWAVES * 64) { const int i = idx - TC_OFF; const bool in = (i >= 0 && i <= 256); const int bk = in ? t5_bucket(i - 128) : 0;
; #pragma unroll
;             for (int j = 0; j < 4; ++j) tab4[j * TC_LEN + idx] = in ? (rel_bias[(4 * kvh + j) * 32 + bk] * LOG2E + 64.0f) * KAPPA : -1.0f; }
; #pragma unroll
;         for (int half = 0; half < 2; ++half) {
;             v4u kv[4], vv[4];
; #pragma unroll
;             for (int i = 0; i < 4; ++i) { const int c = tid + 512 * (4 * half + i), rw = c >> 3, ch = c & 7, key = w0 + rw; const bool ok = key >= 0 && key < SEQ; const size_t ro = (tb0 + (ok ? key : 0)) * 256 + kvh * 64 + 8 * ch;
;                 kv[i] = *(const v4u*)(CK + ro); vv[i] = *(const v4u*)(CV + ro); }
; #pragma unroll
;             for (int i = 0; i < 4; ++i) { const int c = tid + 512 * (4 * half + i), rw = c >> 3, ch = c & 7;
;                 *(LAS v4u*)(kimg + rw * 128 + ((ch ^ (rw & 7)) * 16)) = kv[i]; *(LAS v4u*)(vimg + rw * 128 + ch * 16) = vv[i]; }
;         }
;         __syncthreads();
.LBB0_1131:
	s_or_b64 exec, exec, s[22:23]
	s_addk_i32 s41, 0xff80
	v_add_u32_e32 v2, s41, v157
	v_cmp_gt_u32_e32 vcc, s34, v2
	v_add_u32_e32 v5, s41, v158
	v_readlane_b32 s8, v255, 9
	v_cndmask_b32_e32 v8, 0, v2, vcc
	v_cmp_gt_u32_e32 vcc, s34, v5
	v_ashrrev_i32_e32 v9, 31, v8
	v_lshl_add_u64 v[8:9], s[10:11], 0, v[8:9]
	v_cndmask_b32_e32 v16, 0, v5, vcc
	v_add_u32_e32 v5, s41, v159
	v_cmp_gt_u32_e32 vcc, s34, v5
	v_ashrrev_i32_e32 v17, 31, v16
	v_lshlrev_b64 v[8:9], 9, v[8:9]
	v_cndmask_b32_e32 v24, 0, v5, vcc
	v_add_u32_e32 v5, s41, v160
	v_cmp_gt_u32_e32 vcc, s34, v5
	v_lshl_or_b32 v2, s40, 7, v182
	v_lshl_add_u64 v[16:17], s[10:11], 0, v[16:17]
	v_cndmask_b32_e32 v32, 0, v5, vcc
	v_add_u32_e32 v5, s41, v165
	v_cmp_gt_u32_e32 vcc, s34, v5
	v_ashrrev_i32_e32 v25, 31, v24
	v_or_b32_e32 v8, v8, v2
	v_cndmask_b32_e32 v40, 0, v5, vcc
	v_add_u32_e32 v5, s41, v166
	v_cmp_gt_u32_e32 vcc, s34, v5
	v_readlane_b32 s9, v255, 10
	v_lshlrev_b64 v[16:17], 9, v[16:17]
	v_cndmask_b32_e32 v48, 0, v5, vcc
	v_add_u32_e32 v5, s41, v167
	v_lshl_add_u64 v[24:25], s[10:11], 0, v[24:25]
	v_ashrrev_i32_e32 v33, 31, v32
	v_cmp_gt_u32_e32 vcc, s34, v5
	v_lshl_add_u64 v[10:11], s[8:9], 0, v[8:9]
	v_lshl_add_u64 v[12:13], s[12:13], 0, v[8:9]
	v_or_b32_e32 v16, v16, v2
	v_lshlrev_b64 v[24:25], 9, v[24:25]
	v_lshl_add_u64 v[32:33], s[10:11], 0, v[32:33]
	v_ashrrev_i32_e32 v41, 31, v40
	v_cndmask_b32_e32 v56, 0, v5, vcc
	v_add_u32_e32 v5, s41, v168
	global_load_dwordx4 v[8:11], v[10:11], off
	s_nop 0
	global_load_dwordx4 v[12:15], v[12:13], off
	v_lshl_add_u64 v[18:19], s[8:9], 0, v[16:17]
	v_lshl_add_u64 v[20:21], s[12:13], 0, v[16:17]
	v_or_b32_e32 v24, v24, v2
	v_lshlrev_b64 v[32:33], 9, v[32:33]
	v_lshl_add_u64 v[40:41], s[10:11], 0, v[40:41]
	v_ashrrev_i32_e32 v49, 31, v48
	v_cmp_gt_u32_e32 vcc, s34, v5
	global_load_dwordx4 v[16:19], v[18:19], off
	s_nop 0
	global_load_dwordx4 v[20:23], v[20:21], off
	v_lshl_add_u64 v[26:27], s[8:9], 0, v[24:25]
	v_lshl_add_u64 v[28:29], s[12:13], 0, v[24:25]
	v_or_b32_e32 v32, v32, v2
	v_lshlrev_b64 v[40:41], 9, v[40:41]
	v_lshl_add_u64 v[48:49], s[10:11], 0, v[48:49]
	v_ashrrev_i32_e32 v57, 31, v56
	v_cndmask_b32_e32 v64, 0, v5, vcc
	global_load_dwordx4 v[24:27], v[26:27], off
	s_nop 0
	global_load_dwordx4 v[28:31], v[28:29], off
	v_lshl_add_u64 v[34:35], s[8:9], 0, v[32:33]
	v_lshl_add_u64 v[36:37], s[12:13], 0, v[32:33]
	v_or_b32_e32 v40, v40, v2
	v_lshlrev_b64 v[48:49], 9, v[48:49]
	v_lshl_add_u64 v[56:57], s[10:11], 0, v[56:57]
	v_ashrrev_i32_e32 v65, 31, v64
	global_load_dwordx4 v[32:35], v[34:35], off
	s_nop 0
	global_load_dwordx4 v[36:39], v[36:37], off
	v_lshl_add_u64 v[42:43], s[8:9], 0, v[40:41]
	v_lshl_add_u64 v[44:45], s[12:13], 0, v[40:41]
	v_or_b32_e32 v48, v48, v2
	v_lshlrev_b64 v[56:57], 9, v[56:57]
	v_lshl_add_u64 v[64:65], s[10:11], 0, v[64:65]
	global_load_dwordx4 v[40:43], v[42:43], off
	s_nop 0
	global_load_dwordx4 v[44:47], v[44:45], off
	v_lshl_add_u64 v[50:51], s[8:9], 0, v[48:49]
	v_lshl_add_u64 v[52:53], s[12:13], 0, v[48:49]
	v_or_b32_e32 v56, v56, v2
	v_lshlrev_b64 v[68:69], 9, v[64:65]
	global_load_dwordx4 v[48:51], v[50:51], off
	s_nop 0
	global_load_dwordx4 v[52:55], v[52:53], off
	v_lshl_add_u64 v[58:59], s[8:9], 0, v[56:57]
	v_lshl_add_u64 v[60:61], s[12:13], 0, v[56:57]
	v_or_b32_e32 v68, v68, v2
	global_load_dwordx4 v[56:59], v[58:59], off
	s_nop 0
	global_load_dwordx4 v[60:63], v[60:61], off
	v_lshl_add_u64 v[64:65], s[8:9], 0, v[68:69]
	v_lshl_add_u64 v[68:69], s[12:13], 0, v[68:69]
	global_load_dwordx4 v[64:67], v[64:65], off
	v_add_u32_e32 v2, v143, v161
	global_load_dwordx4 v[68:71], v[68:69], off
	s_sub_i32 s8, 0x80, s33
	s_lshl_b32 s24, s40, 2
	s_lshr_b32 s11, s8, 5
	v_lshlrev_b64 v[6:7], 10, v[6:7]
	s_waitcnt vmcnt(16)
	v_mov_b64_e32 v[86:87], v[102:103]
	v_mov_b64_e32 v[90:91], v[106:107]
	v_mov_b64_e32 v[94:95], v[110:111]
	v_mov_b64_e32 v[98:99], v[114:115]
	s_mov_b32 s25, 0
	v_sub_u32_e32 v194, v138, v4
	v_lshl_add_u64 v[146:147], v[140:141], 0, v[6:7]
	v_mov_b64_e32 v[88:89], v[104:105]
	v_mov_b64_e32 v[92:93], v[108:109]
	v_mov_b64_e32 v[96:97], v[112:113]
	v_mov_b64_e32 v[100:101], v[116:117]
	s_waitcnt vmcnt(15)
	ds_write_b128 v183, v[8:11] offset:6144
	s_waitcnt vmcnt(14)
	ds_write_b128 v2, v[12:15]
	s_waitcnt vmcnt(13)
	ds_write_b128 v184, v[16:19] offset:6144
	v_add_u32_e32 v2, v143, v162
	s_waitcnt vmcnt(12)
	ds_write_b128 v2, v[20:23]
	s_waitcnt vmcnt(11)
	ds_write_b128 v185, v[24:27] offset:6144
	v_add_u32_e32 v2, v143, v163
	s_waitcnt vmcnt(10)
	ds_write_b128 v2, v[28:31]
	s_waitcnt vmcnt(9)
	ds_write_b128 v186, v[32:35] offset:6144
	v_add_u32_e32 v2, v143, v164
	s_waitcnt vmcnt(8)
	ds_write_b128 v2, v[36:39]
	s_waitcnt vmcnt(7)
	ds_write_b128 v187, v[40:43] offset:6144
	v_add_u32_e32 v2, v143, v169
	s_waitcnt vmcnt(6)
	ds_write_b128 v2, v[44:47]
	s_waitcnt vmcnt(5)
	ds_write_b128 v188, v[48:51] offset:6144
	v_add_u32_e32 v2, v143, v170
	s_waitcnt vmcnt(4)
	ds_write_b128 v2, v[52:55]
	s_waitcnt vmcnt(3)
	ds_write_b128 v189, v[56:59] offset:6144
	v_add_u32_e32 v2, v143, v171
	s_waitcnt vmcnt(2)
	ds_write_b128 v2, v[60:63]
	s_waitcnt vmcnt(1)
	ds_write_b128 v190, v[64:67] offset:6144
	v_add_u32_e32 v2, v143, v172
	s_waitcnt vmcnt(0)
	ds_write_b128 v2, v[68:71]
	v_sub_co_u32_e32 v2, vcc, s33, v191
	s_and_b64 s[8:9], vcc, exec
	s_cselect_b32 s26, s11, 0
	s_sub_i32 s8, 0x2080, s33
	s_ashr_i32 s8, s8, 5
	s_min_i32 s27, s8, 9
	s_add_i32 s8, s26, 1
	s_cmp_lt_i32 s8, s27
	v_readfirstlane_b32 s10, v2
	s_cselect_b64 s[22:23], -1, 0
	s_lshl_b32 s8, s26, 7
	s_lshl_b32 s28, s26, 12
	v_add_u32_e32 v195, s8, v175
	v_add_u32_e32 v196, s8, v174
	v_add_u32_e32 v197, s28, v176
	v_add_u32_e32 v198, s28, v177
	v_add_u32_e32 v199, s28, v178
	v_add_u32_e32 v200, s28, v179
	v_add_u32_e32 v201, s28, v180
	s_lshl_b32 s29, s10, 2
	s_waitcnt lgkmcnt(0)
	s_barrier
